# c22: c13 with 32 bytes of padding after phase 4 so that the attention, branch-merge, output-projection and expert-GEMM loops sit at the baseline's byte phase modulo 128 (code placement)
# baseline (speedup 1.0000x reference)
.LBB0_650:
	s_nop 0
	s_nop 0
	s_nop 0
	s_nop 0
	s_nop 0
	s_nop 0
	s_nop 0
	s_nop 0
	s_load_dwordx2 s[0:1], s[96:97], 0xe8
	s_waitcnt lgkmcnt(0)
	s_cmp_gt_i32 s1, 5
	s_cselect_b64 s[0:1], -1, 0
	s_and_b64 s[2:3], s[40:41], s[0:1]
	s_andn2_b64 vcc, exec, s[2:3]
	s_cbranch_vccnz .LBB0_704
	s_waitcnt vmcnt(0)
	s_waitcnt vmcnt(0)
	s_barrier
	s_mov_b64 s[4:5], exec
	v_readlane_b32 s2, v249, 34
	v_readlane_b32 s3, v249, 35
	s_and_b64 s[2:3], s[4:5], s[2:3]
	s_mov_b64 exec, s[2:3]
	s_cbranch_execz .LBB0_703
	s_add_i32 s2, 0, 0x27800
	v_mov_b32_e32 v1, s2
	s_waitcnt vmcnt(0) expcnt(0) lgkmcnt(0)
	ds_read_b32 v3, v1
	s_add_i32 s2, 0, 0x27804
	v_mov_b32_e32 v1, s2
	ds_read_b32 v1, v1
	s_waitcnt lgkmcnt(1)
	v_cmp_ne_u32_e32 vcc, 0, v3
	s_cbranch_vccnz .LBB0_667
	v_readlane_b32 s6, v249, 10
	v_readlane_b32 s7, v249, 11
	s_load_dwordx2 s[2:3], s[6:7], 0x4
	s_add_u32 s6, s50, 0x4200
	s_addc_u32 s7, s51, 0
	s_add_u32 s8, s50, 0x4400
	s_addc_u32 s9, s51, 0
	v_readlane_b32 s10, v249, 12
	v_readlane_b32 s11, v249, 13
	s_waitcnt lgkmcnt(0)
	s_mul_i32 s2, s2, s10
	s_add_u32 s10, s50, 0x4500
	s_addc_u32 s11, s51, 0
	s_add_u32 s12, s50, 0x4600
	s_addc_u32 s13, s51, 0
	s_add_u32 s14, s50, 0x4700
	s_addc_u32 s15, s51, 0
	s_add_u32 s16, s50, 0x4800
	s_addc_u32 s17, s51, 0
	s_add_u32 s18, s50, 0x4900
	s_addc_u32 s19, s51, 0
	s_add_u32 s20, s50, 0x4a00
	s_addc_u32 s21, s51, 0
	s_add_u32 s22, s50, 0x4b00
	s_addc_u32 s23, s51, 0
	s_add_u32 s24, s50, 0x4c00
	s_addc_u32 s25, s51, 0
	s_add_u32 s26, s50, 0x4d00
	s_addc_u32 s27, s51, 0
	s_add_u32 s28, s50, 0x4e00
	s_addc_u32 s29, s51, 0
	s_add_u32 s30, s50, 0x4f00
	s_addc_u32 s31, s51, 0
	s_add_u32 s34, s50, 0x5000
	s_addc_u32 s35, s51, 0
	s_add_u32 s36, s50, 0x5100
	s_addc_u32 s37, s51, 0
	s_add_u32 s38, s50, 0x5200
	s_addc_u32 s39, s51, 0
	s_add_u32 s40, s50, 0x5300
	s_mul_i32 s2, s2, s3
	s_addc_u32 s41, s51, 0
	s_mov_b32 s3, 1
	v_mov_b32_e32 v17, 0
	s_branch .LBB0_655
